# speedup vs baseline: 1.0249x; 1.0249x over previous
.Lat_spec_ok:
	v_and_b32_e32 v31, 7, v0
	v_bitop3_b32 v33, v10, v0, 7 bitop3:0x78
	v_lshlrev_b32_e32 v1, 7, v1
	v_mbcnt_lo_u32_b32 v34, -1, 0
	v_lshlrev_b32_e32 v89, 4, v33
	v_bitop3_b32 v31, v10, v31, 4 bitop3:0x36
	v_xor_b32_e32 v33, v13, v0
	v_mov_b32_e32 v13, v12
	v_lshlrev_b32_e32 v87, 4, v11
	s_movk_i32 s1, 0x70
	v_lshlrev_b32_e32 v98, 2, v10
	v_mov_b32_e32 v10, v12
	v_mov_b32_e32 v11, v12
	v_mbcnt_hi_u32_b32 v0, -1, v34
	v_lshl_or_b32 v91, v31, 4, v1
	v_lshlrev_b32_e32 v31, 4, v33
	v_mov_b64_e32 v[36:37], v[12:13]
	v_mov_b64_e32 v[40:41], v[12:13]
	v_mov_b64_e32 v[44:45], v[12:13]
	v_mov_b64_e32 v[48:49], v[12:13]
	v_mov_b64_e32 v[52:53], v[12:13]
	s_mov_b32 s17, 0
	v_mov_b64_e32 v[100:101], 0
	s_mov_b64 s[14:15], -1
	s_mov_b32 s5, 0xff800000
	s_mov_b32 s7, 0x41000000
	s_mov_b32 s12, 0x3c003c00
	v_mov_b32_e32 v30, 0x3c003c00
	v_mov_b32_e32 v114, v30
	v_mov_b32_e32 v115, v30
	v_mov_b32_e32 v116, v30
	v_mov_b32_e32 v117, v30
	v_mov_b32_e32 v120, v12
	v_mov_b32_e32 v121, v12
	v_mov_b32_e32 v122, v12
	v_mov_b32_e32 v123, v12
	v_mov_b64_e32 v[34:35], v[10:11]
	v_mov_b64_e32 v[38:39], v[10:11]
	v_mov_b64_e32 v[42:43], v[10:11]
	v_mov_b64_e32 v[46:47], v[10:11]
	v_mov_b64_e32 v[50:51], v[10:11]
	v_and_or_b32 v99, v31, s1, v32
	s_mov_b32 s9, 0
	s_waitcnt vmcnt(3)
	ds_write_b128 v99, v[22:25]
	ds_write_b128 v90, v[14:17] offset:8192
	s_waitcnt vmcnt(2)
	ds_write_b128 v99, v[18:21] offset:4096
	s_waitcnt vmcnt(1)
	ds_write_b128 v90, v[26:29] offset:12288
	s_waitcnt vmcnt(0)
.LBB1_17:
.LBB1_20:
	s_and_b32 s22, s8, 0x11111111
	s_and_b32 s23, s8, 0x22222222
	s_cmp_lg_u32 s22, 0
	s_cselect_b32 s22, s22, s23
	s_and_b32 s23, s8, 0x44444444
	s_cmp_lg_u32 s22, 0
	s_cselect_b32 s22, s22, s23
	s_and_b32 s23, s8, 0x88888888
	s_cmp_lg_u32 s22, 0
	s_cselect_b32 s22, s22, s23
	s_ff1_i32_b32 s16, s22
	s_cmp_lg_u32 s22, 0
	s_cselect_b64 s[18:19], -1, 0
	s_cbranch_scc0 .LBB1_27
	s_bitset0_b32 s8, s16
	s_lshl_b32 s22, s16, 13
	s_add_u32 s24, s86, s22
	s_addc_u32 s25, s87, 0
	s_add_u32 s26, s84, s22
	s_addc_u32 s27, s85, 0
	s_lshl_b32 s22, s16, 14
	s_add_u32 s28, s88, s22
	s_addc_u32 s29, s89, 0
	global_load_dwordx4 v[14:17], v90, s[24:25]
	global_load_dwordx4 v[22:25], v90, s[26:27]
	global_load_dwordx4 v[18:21], v119, s[26:27]
	global_load_dwordx4 v[26:29], v119, s[24:25]
	global_load_dwordx2 v[100:101], v118, s[28:29]

.LBB1_44:
	v_exp_f32_e32 v10, v68
	v_exp_f32_e32 v11, v69
	v_exp_f32_e32 v32, v64
	v_exp_f32_e32 v13, v70
	v_exp_f32_e32 v31, v71
	v_cvt_pkrtz_f16_f32 v64, v10, v11
	v_add_u32_e32 v10, s10, v87
	ds_read_b128 v[72:75], v10 offset:8192
	ds_read_b128 v[76:79], v10 offset:10240
	v_exp_f32_e32 v33, v65
	v_exp_f32_e32 v54, v66
	v_exp_f32_e32 v55, v67
	ds_read_b128 v[80:83], v10 offset:12288
	ds_read_b128 v[106:109], v10 offset:9216
	v_cvt_pkrtz_f16_f32 v65, v13, v31
	v_cvt_pkrtz_f16_f32 v67, v54, v55
	v_cvt_pkrtz_f16_f32 v66, v32, v33
	v_exp_f32_e32 v84, v60
	v_exp_f32_e32 v85, v61
	v_exp_f32_e32 v11, v62
	s_waitcnt lgkmcnt(3)
	v_mfma_f32_16x16x32_f16 v[46:49], v[72:75], v[64:67], v[46:49]
	v_exp_f32_e32 v13, v63
	ds_read_b128 v[60:63], v10 offset:14336
	ds_read_b128 v[110:113], v10 offset:11264
	v_exp_f32_e32 v31, v56
	s_waitcnt lgkmcnt(4)
	v_mfma_f32_16x16x32_f16 v[42:45], v[76:79], v[64:67], v[42:45]
	v_exp_f32_e32 v72, v57
	ds_read_b128 v[54:57], v10 offset:13312
	v_exp_f32_e32 v73, v58
	s_waitcnt lgkmcnt(4)
	v_mfma_f32_16x16x32_f16 v[38:41], v[80:83], v[64:67], v[38:41]
	ds_read_b128 v[78:81], v10 offset:15360
	v_exp_f32_e32 v74, v59
	v_cvt_pkrtz_f16_f32 v58, v84, v85
	v_mfma_f32_16x16x32_f16 v[50:53], v[114:117], v[64:67], v[50:53]
	v_cvt_pkrtz_f16_f32 v59, v11, v13
	s_waitcnt lgkmcnt(3)
	v_mfma_f32_16x16x32_f16 v[34:37], v[60:63], v[64:67], v[34:37]
	v_cvt_pkrtz_f16_f32 v61, v73, v74
	v_cvt_pkrtz_f16_f32 v60, v31, v72
	s_nop 1
	v_mfma_f32_16x16x32_f16 v[50:53], v[114:117], v[58:61], v[50:53]
	v_mfma_f32_16x16x32_f16 v[46:49], v[106:109], v[58:61], v[46:49]
	s_waitcnt lgkmcnt(2)
	v_mfma_f32_16x16x32_f16 v[42:45], v[110:113], v[58:61], v[42:45]
	s_waitcnt lgkmcnt(1)
	v_mfma_f32_16x16x32_f16 v[38:41], v[54:57], v[58:61], v[38:41]
	s_waitcnt lgkmcnt(0)
	v_mfma_f32_16x16x32_f16 v[34:37], v[78:81], v[58:61], v[34:37]
	s_andn2_b64 vcc, exec, s[18:19]
	s_cbranch_vccnz .Lat_exit4
	s_xor_b32 s9, s9, 1
	s_lshl_b32 s10, s9, 14
	s_waitcnt vmcnt(0)
	v_or_b32_e32 v10, s10, v99
	v_mov_b64_e32 v[102:103], v[100:101]
	v_or_b32_e32 v11, s10, v90
	ds_write_b128 v10, v[22:25]
	ds_write_b128 v11, v[14:17] offset:8192
	ds_write_b128 v10, v[18:21] offset:4096
	ds_write_b128 v11, v[26:29] offset:12288
	s_mov_b64 s[14:15], s[0:1]
	s_mov_b32 s0, s16
	s_branch .LBB1_20

.LBB1_46:
	v_mov_b64_e32 v[34:35], v[58:59]
	v_mov_b64_e32 v[38:39], v[62:63]
	v_mov_b64_e32 v[42:43], v[66:67]
	v_mov_b64_e32 v[46:47], v[70:71]
	v_mov_b64_e32 v[50:51], v[74:75]
	s_mov_b64 s[14:15], s[0:1]
	v_mov_b64_e32 v[36:37], v[60:61]
	v_mov_b64_e32 v[40:41], v[64:65]
	v_mov_b64_e32 v[44:45], v[68:69]
	v_mov_b64_e32 v[48:49], v[72:73]
	v_mov_b64_e32 v[52:53], v[76:77]
	s_mov_b32 s0, s16
	s_waitcnt vmcnt(0)
	v_mov_b64_e32 v[100:101], v[102:103]
	s_branch .LBB1_20
